# v5 + softmax row-max exchange between lane halves by v_permlane32_swap instead of ds_bpermute (P4 tile loop 2 sites, P12 5 sites), bit-identical
# baseline (speedup 1.0000x reference)
.LBB0_547:
	v_add_u32_e32 v2, s62, v147
	v_add_u32_e32 v214, v2, v155
	ds_read_b128 v[214:217], v214 offset:57600
	s_waitcnt lgkmcnt(0)
	v_mfma_f32_32x32x16_bf16 v[70:85], v[214:217], v[86:89], v[70:85]
	v_add_u32_e32 v214, v2, v157
	ds_read_b128 v[214:217], v214 offset:57600
	s_waitcnt lgkmcnt(0)
	v_mfma_f32_32x32x16_bf16 v[70:85], v[214:217], v[90:93], v[70:85]
	v_add_u32_e32 v214, v2, v170
	ds_read_b128 v[214:217], v214 offset:57600
	s_waitcnt lgkmcnt(0)
	v_mfma_f32_32x32x16_bf16 v[70:85], v[214:217], v[94:97], v[70:85]
	v_add_u32_e32 v214, v2, v171
	ds_read_b128 v[214:217], v214 offset:57600
	s_waitcnt lgkmcnt(0)
	v_mfma_f32_32x32x16_bf16 v[70:85], v[214:217], v[98:101], v[70:85]
	v_add_u32_e32 v214, v2, v172
	ds_read_b128 v[214:217], v214 offset:57600
	s_waitcnt lgkmcnt(0)
	v_mfma_f32_32x32x16_bf16 v[70:85], v[214:217], v[102:105], v[70:85]
	v_add_u32_e32 v214, v2, v173
	ds_read_b128 v[214:217], v214 offset:57600
	s_waitcnt lgkmcnt(0)
	v_mfma_f32_32x32x16_bf16 v[70:85], v[214:217], v[106:109], v[70:85]
	v_add_u32_e32 v214, v2, v174
	ds_read_b128 v[214:217], v214 offset:57600
	v_add_u32_e32 v2, v2, v175
	s_waitcnt lgkmcnt(0)
	v_mfma_f32_32x32x16_bf16 v[70:85], v[214:217], v[110:113], v[70:85]
	ds_read_b128 v[214:217], v2 offset:57600
	v_add_u32_e32 v2, 0, v212
	ds_read_b32 v2, v2
	s_waitcnt lgkmcnt(0)
	v_lshrrev_b32_e32 v2, v122, v2
	v_mfma_f32_32x32x16_bf16 v[70:85], v[214:217], v[114:117], v[70:85]
	v_bfe_i32 v214, v2, 0, 1
	s_nop 10
	v_bitop3_b32 v221, v70, s53, v214 bitop3:0xe4
	v_bfe_i32 v70, v2, 1, 1
	v_bitop3_b32 v220, v71, s53, v70 bitop3:0xe4
	v_bfe_i32 v71, v2, 2, 1
	v_bitop3_b32 v219, v72, s53, v71 bitop3:0xe4
	v_bfe_i32 v71, v2, 3, 1
	v_bitop3_b32 v218, v73, s53, v71 bitop3:0xe4
	v_bfe_i32 v71, v2, 4, 1
	v_bitop3_b32 v217, v74, s53, v71 bitop3:0xe4
	v_bfe_i32 v71, v2, 5, 1
	v_bitop3_b32 v216, v75, s53, v71 bitop3:0xe4
	v_bfe_i32 v71, v2, 6, 1
	v_bitop3_b32 v215, v76, s53, v71 bitop3:0xe4
	v_bfe_i32 v71, v2, 7, 1
	v_bitop3_b32 v214, v77, s53, v71 bitop3:0xe4
	v_bfe_i32 v71, v2, 16, 1
	v_max3_f32 v70, v221, s54, v220
	v_bitop3_b32 v77, v78, s53, v71 bitop3:0xe4
	v_bfe_i32 v71, v2, 17, 1
	v_max3_f32 v70, v70, v219, v218
	v_bitop3_b32 v76, v79, s53, v71 bitop3:0xe4
	v_bfe_i32 v71, v2, 18, 1
	v_max3_f32 v70, v70, v217, v216
	v_bitop3_b32 v75, v80, s53, v71 bitop3:0xe4
	v_bfe_i32 v71, v2, 19, 1
	v_max3_f32 v70, v70, v215, v214
	v_bitop3_b32 v74, v81, s53, v71 bitop3:0xe4
	v_bfe_i32 v71, v2, 20, 1
	v_max3_f32 v70, v70, v77, v76
	v_bitop3_b32 v73, v82, s53, v71 bitop3:0xe4
	v_bfe_i32 v71, v2, 21, 1
	v_max3_f32 v70, v70, v75, v74
	v_bitop3_b32 v72, v83, s53, v71 bitop3:0xe4
	v_max3_f32 v78, v70, v73, v72
	v_bfe_i32 v70, v2, 22, 1
	v_bfe_i32 v2, v2, 23, 1
	v_bitop3_b32 v71, v84, s53, v70 bitop3:0xe4
	v_bitop3_b32 v70, v85, s53, v2 bitop3:0xe4
	v_and_b32_e32 v79, 64, v209
	v_max3_f32 v2, v78, v71, v70
	v_add_u32_e32 v79, 64, v79
	v_mov_b32_e32 v78, v2
	s_nop 1
	v_permlane32_swap_b32 v78, v2
	s_waitcnt lgkmcnt(0)
	v_max3_f32 v2, v213, v2, v78
	v_cmp_eq_f32_e32 vcc, v2, v213
	s_cmp_eq_u64 vcc, exec
	s_cbranch_scc1 .LBB0_549
	v_sub_f32_e32 v78, v213, v2
	v_exp_f32_e32 v78, v78
	s_nop 0
	v_pk_mul_f32 v[66:67], v[66:67], v[78:79] op_sel_hi:[1,0]
	v_pk_mul_f32 v[64:65], v[64:65], v[78:79] op_sel_hi:[1,0]
	v_pk_mul_f32 v[62:63], v[62:63], v[78:79] op_sel_hi:[1,0]
	v_pk_mul_f32 v[60:61], v[60:61], v[78:79] op_sel_hi:[1,0]
	v_pk_mul_f32 v[58:59], v[58:59], v[78:79] op_sel_hi:[1,0]
	v_pk_mul_f32 v[56:57], v[56:57], v[78:79] op_sel_hi:[1,0]
	v_pk_mul_f32 v[54:55], v[54:55], v[78:79] op_sel_hi:[1,0]
	v_pk_mul_f32 v[52:53], v[52:53], v[78:79] op_sel_hi:[1,0]
	v_pk_mul_f32 v[50:51], v[50:51], v[78:79] op_sel_hi:[1,0]
	v_pk_mul_f32 v[48:49], v[48:49], v[78:79] op_sel_hi:[1,0]
	v_pk_mul_f32 v[46:47], v[46:47], v[78:79] op_sel_hi:[1,0]
	v_pk_mul_f32 v[44:45], v[44:45], v[78:79] op_sel_hi:[1,0]
	v_pk_mul_f32 v[42:43], v[42:43], v[78:79] op_sel_hi:[1,0]
	v_pk_mul_f32 v[40:41], v[40:41], v[78:79] op_sel_hi:[1,0]
	v_pk_mul_f32 v[38:39], v[38:39], v[78:79] op_sel_hi:[1,0]
	v_pk_mul_f32 v[36:37], v[36:37], v[78:79] op_sel_hi:[1,0]
	v_pk_mul_f32 v[34:35], v[34:35], v[78:79] op_sel_hi:[1,0]
	v_pk_mul_f32 v[32:33], v[32:33], v[78:79] op_sel_hi:[1,0]
	v_pk_mul_f32 v[30:31], v[30:31], v[78:79] op_sel_hi:[1,0]
	v_pk_mul_f32 v[28:29], v[28:29], v[78:79] op_sel_hi:[1,0]
	v_pk_mul_f32 v[26:27], v[26:27], v[78:79] op_sel_hi:[1,0]
	v_pk_mul_f32 v[24:25], v[24:25], v[78:79] op_sel_hi:[1,0]
	v_pk_mul_f32 v[22:23], v[22:23], v[78:79] op_sel_hi:[1,0]
	v_pk_mul_f32 v[20:21], v[20:21], v[78:79] op_sel_hi:[1,0]
	v_pk_mul_f32 v[18:19], v[18:19], v[78:79] op_sel_hi:[1,0]
	v_pk_mul_f32 v[16:17], v[16:17], v[78:79] op_sel_hi:[1,0]
	v_pk_mul_f32 v[14:15], v[14:15], v[78:79] op_sel_hi:[1,0]
	v_pk_mul_f32 v[12:13], v[12:13], v[78:79] op_sel_hi:[1,0]
	v_pk_mul_f32 v[10:11], v[10:11], v[78:79] op_sel_hi:[1,0]
	v_pk_mul_f32 v[8:9], v[8:9], v[78:79] op_sel_hi:[1,0]
	v_pk_mul_f32 v[6:7], v[6:7], v[78:79] op_sel_hi:[1,0]
	v_pk_mul_f32 v[4:5], v[4:5], v[78:79] op_sel_hi:[1,0]
	v_mul_f32_e32 v68, v68, v78

.LBB0_554:
	s_or_b32 s6, s62, 0x2000
	v_add_u32_e32 v213, s6, v177
	ds_read_b128 v[214:217], v213
	v_add_u32_e32 v213, s6, v181
	s_waitcnt lgkmcnt(0)
	v_mfma_f32_32x32x16_bf16 v[70:85], v[214:217], v[86:89], v[70:85]
	ds_read_b128 v[214:217], v213
	v_add_u32_e32 v213, s6, v183
	s_waitcnt lgkmcnt(0)
	v_mfma_f32_32x32x16_bf16 v[70:85], v[214:217], v[90:93], v[70:85]
	ds_read_b128 v[214:217], v213
	v_add_u32_e32 v213, s6, v184
	s_waitcnt lgkmcnt(0)
	v_mfma_f32_32x32x16_bf16 v[70:85], v[214:217], v[94:97], v[70:85]
	ds_read_b128 v[214:217], v213
	v_add_u32_e32 v213, s6, v185
	s_waitcnt lgkmcnt(0)
	v_mfma_f32_32x32x16_bf16 v[70:85], v[214:217], v[98:101], v[70:85]
	ds_read_b128 v[214:217], v213
	v_add_u32_e32 v213, s6, v186
	s_waitcnt lgkmcnt(0)
	v_mfma_f32_32x32x16_bf16 v[70:85], v[214:217], v[102:105], v[70:85]
	ds_read_b128 v[214:217], v213
	v_add_u32_e32 v213, s6, v187
	s_waitcnt lgkmcnt(0)
	v_mfma_f32_32x32x16_bf16 v[70:85], v[214:217], v[106:109], v[70:85]
	ds_read_b128 v[214:217], v213
	v_add_u32_e32 v213, s6, v188
	s_waitcnt lgkmcnt(0)
	v_mfma_f32_32x32x16_bf16 v[70:85], v[214:217], v[110:113], v[70:85]
	ds_read_b128 v[214:217], v213
	v_add_u32_e32 v213, 0, v212
	ds_read_b32 v213, v213 offset:4
	s_waitcnt lgkmcnt(0)
	v_lshrrev_b32_e32 v213, v122, v213
	v_mfma_f32_32x32x16_bf16 v[70:85], v[214:217], v[114:117], v[70:85]
	v_bfe_i32 v214, v213, 0, 1
	s_nop 10
	v_bitop3_b32 v221, v70, s53, v214 bitop3:0xe4
	v_bfe_i32 v70, v213, 1, 1
	v_bitop3_b32 v220, v71, s53, v70 bitop3:0xe4
	v_bfe_i32 v71, v213, 2, 1
	v_bitop3_b32 v219, v72, s53, v71 bitop3:0xe4
	v_bfe_i32 v71, v213, 3, 1
	v_bitop3_b32 v218, v73, s53, v71 bitop3:0xe4
	v_bfe_i32 v71, v213, 4, 1
	v_bitop3_b32 v217, v74, s53, v71 bitop3:0xe4
	v_bfe_i32 v71, v213, 5, 1
	v_bitop3_b32 v216, v75, s53, v71 bitop3:0xe4
	v_bfe_i32 v71, v213, 6, 1
	v_bitop3_b32 v215, v76, s53, v71 bitop3:0xe4
	v_bfe_i32 v71, v213, 7, 1
	v_bitop3_b32 v214, v77, s53, v71 bitop3:0xe4
	v_bfe_i32 v71, v213, 16, 1
	v_max3_f32 v70, v221, s54, v220
	v_bitop3_b32 v77, v78, s53, v71 bitop3:0xe4
	v_bfe_i32 v71, v213, 17, 1
	v_max3_f32 v70, v70, v219, v218
	v_bitop3_b32 v76, v79, s53, v71 bitop3:0xe4
	v_bfe_i32 v71, v213, 18, 1
	v_max3_f32 v70, v70, v217, v216
	v_bitop3_b32 v75, v80, s53, v71 bitop3:0xe4
	v_bfe_i32 v71, v213, 19, 1
	v_max3_f32 v70, v70, v215, v214
	v_bitop3_b32 v74, v81, s53, v71 bitop3:0xe4
	v_bfe_i32 v71, v213, 20, 1
	v_max3_f32 v70, v70, v77, v76
	v_bitop3_b32 v73, v82, s53, v71 bitop3:0xe4
	v_bfe_i32 v71, v213, 21, 1
	v_max3_f32 v70, v70, v75, v74
	v_bitop3_b32 v72, v83, s53, v71 bitop3:0xe4
	v_and_b32_e32 v80, 64, v209
	v_max3_f32 v78, v70, v73, v72
	v_bfe_i32 v70, v213, 22, 1
	v_add_u32_e32 v80, 64, v80
	v_bitop3_b32 v71, v84, s53, v70 bitop3:0xe4
	v_bfe_i32 v70, v213, 23, 1
	v_bitop3_b32 v70, v85, s53, v70 bitop3:0xe4
	v_max3_f32 v78, v78, v71, v70
	v_mov_b32_e32 v79, v78
	s_nop 1
	v_permlane32_swap_b32 v79, v78
	s_waitcnt lgkmcnt(0)
	v_max3_f32 v213, v2, v78, v79
	v_cmp_eq_f32_e32 vcc, v213, v2
	s_cmp_eq_u64 vcc, exec
	s_cbranch_scc1 .LBB0_556
	v_sub_f32_e32 v2, v2, v213
	v_exp_f32_e32 v2, v2
	s_nop 0
	v_pk_mul_f32 v[66:67], v[66:67], v[2:3] op_sel_hi:[1,0]
	v_pk_mul_f32 v[64:65], v[64:65], v[2:3] op_sel_hi:[1,0]
	v_pk_mul_f32 v[62:63], v[62:63], v[2:3] op_sel_hi:[1,0]
	v_pk_mul_f32 v[60:61], v[60:61], v[2:3] op_sel_hi:[1,0]
	v_pk_mul_f32 v[58:59], v[58:59], v[2:3] op_sel_hi:[1,0]
	v_pk_mul_f32 v[56:57], v[56:57], v[2:3] op_sel_hi:[1,0]
	v_pk_mul_f32 v[54:55], v[54:55], v[2:3] op_sel_hi:[1,0]
	v_pk_mul_f32 v[52:53], v[52:53], v[2:3] op_sel_hi:[1,0]
	v_pk_mul_f32 v[50:51], v[50:51], v[2:3] op_sel_hi:[1,0]
	v_pk_mul_f32 v[48:49], v[48:49], v[2:3] op_sel_hi:[1,0]
	v_pk_mul_f32 v[46:47], v[46:47], v[2:3] op_sel_hi:[1,0]
	v_pk_mul_f32 v[44:45], v[44:45], v[2:3] op_sel_hi:[1,0]
	v_pk_mul_f32 v[42:43], v[42:43], v[2:3] op_sel_hi:[1,0]
	v_pk_mul_f32 v[40:41], v[40:41], v[2:3] op_sel_hi:[1,0]
	v_pk_mul_f32 v[38:39], v[38:39], v[2:3] op_sel_hi:[1,0]
	v_pk_mul_f32 v[36:37], v[36:37], v[2:3] op_sel_hi:[1,0]
	v_pk_mul_f32 v[34:35], v[34:35], v[2:3] op_sel_hi:[1,0]
	v_pk_mul_f32 v[32:33], v[32:33], v[2:3] op_sel_hi:[1,0]
	v_pk_mul_f32 v[30:31], v[30:31], v[2:3] op_sel_hi:[1,0]
	v_pk_mul_f32 v[28:29], v[28:29], v[2:3] op_sel_hi:[1,0]
	v_pk_mul_f32 v[26:27], v[26:27], v[2:3] op_sel_hi:[1,0]
	v_pk_mul_f32 v[24:25], v[24:25], v[2:3] op_sel_hi:[1,0]
	v_pk_mul_f32 v[22:23], v[22:23], v[2:3] op_sel_hi:[1,0]
	v_pk_mul_f32 v[20:21], v[20:21], v[2:3] op_sel_hi:[1,0]
	v_pk_mul_f32 v[18:19], v[18:19], v[2:3] op_sel_hi:[1,0]
	v_pk_mul_f32 v[16:17], v[16:17], v[2:3] op_sel_hi:[1,0]
	v_pk_mul_f32 v[14:15], v[14:15], v[2:3] op_sel_hi:[1,0]
	v_pk_mul_f32 v[12:13], v[12:13], v[2:3] op_sel_hi:[1,0]
	v_pk_mul_f32 v[10:11], v[10:11], v[2:3] op_sel_hi:[1,0]
	v_pk_mul_f32 v[8:9], v[8:9], v[2:3] op_sel_hi:[1,0]
	v_pk_mul_f32 v[6:7], v[6:7], v[2:3] op_sel_hi:[1,0]
	v_pk_mul_f32 v[4:5], v[4:5], v[2:3] op_sel_hi:[1,0]
	v_mul_f32_e32 v68, v68, v2

.LBB0_1379:
	v_or_b32_e32 v18, s18, v151
	v_lshrrev_b32_e32 v27, 1, v18
	v_lshl_add_u32 v26, v18, 7, 0
	v_bitop3_b32 v18, v27, v53, 7 bitop3:0x6c
	v_lshl_add_u32 v18, v18, 4, v26
	ds_read_b128 v[18:21], v18
	v_add_u32_e32 v22, 2, v53
	v_bitop3_b32 v22, v27, v22, 7 bitop3:0x6c
	v_lshl_add_u32 v22, v22, 4, v26
	ds_read_b128 v[22:25], v22
	v_add_u32_e32 v28, -1, v159
	v_cmp_gt_u32_e32 vcc, s51, v159
	v_add_u32_e32 v29, -16, v159
	s_waitcnt lgkmcnt(1)
	v_mfma_f32_32x32x16_bf16 v[2:17], v[18:21], v[128:131], v[2:17]
	v_add_u32_e32 v18, 4, v53
	v_bitop3_b32 v18, v27, v18, 7 bitop3:0x6c
	v_lshl_add_u32 v18, v18, 4, v26
	ds_read_b128 v[18:21], v18
	s_waitcnt lgkmcnt(1)
	v_mfma_f32_32x32x16_bf16 v[2:17], v[22:25], v[136:139], v[2:17]
	v_add_u32_e32 v22, 6, v53
	v_bitop3_b32 v22, v27, v22, 7 bitop3:0x6c
	v_lshl_add_u32 v22, v22, 4, v26
	ds_read_b128 v[22:25], v22
	v_add_u32_e32 v26, -6, v159
	v_add_u32_e32 v27, -7, v159
	s_waitcnt lgkmcnt(1)
	v_mfma_f32_32x32x16_bf16 v[2:17], v[18:21], v[140:143], v[2:17]
	v_add_u32_e32 v18, -2, v159
	v_add_u32_e32 v19, -3, v159
	v_add_u32_e32 v20, -4, v159
	v_add_u32_e32 v21, -5, v159
	s_waitcnt lgkmcnt(0)
	v_mfma_f32_32x32x16_bf16 v[2:17], v[22:25], v[132:135], v[2:17]
	s_nop 11
	v_cndmask_b32_e32 v2, v221, v2, vcc
	v_cmp_gt_u32_e32 vcc, s51, v28
	s_nop 1
	v_cndmask_b32_e32 v3, v221, v3, vcc
	v_cmp_gt_u32_e32 vcc, s51, v18
	v_max3_f32 v18, v2, s60, v3
	s_nop 0
	v_cndmask_b32_e32 v4, v221, v4, vcc
	v_cmp_gt_u32_e32 vcc, s51, v19
	v_subrev_u32_e32 v19, 17, v159
	s_nop 0
	v_cndmask_b32_e32 v5, v221, v5, vcc
	v_cmp_gt_u32_e32 vcc, s51, v20
	v_max3_f32 v18, v18, v4, v5
	s_nop 0
	v_cndmask_b32_e32 v6, v221, v6, vcc
	v_cmp_gt_u32_e32 vcc, s51, v21
	s_nop 1
	v_cndmask_b32_e32 v7, v221, v7, vcc
	v_cmp_gt_u32_e32 vcc, s51, v26
	v_max3_f32 v18, v18, v6, v7
	s_nop 0
	v_cndmask_b32_e32 v8, v221, v8, vcc
	v_cmp_gt_u32_e32 vcc, s51, v27
	s_nop 1
	v_cndmask_b32_e32 v9, v221, v9, vcc
	v_cmp_gt_u32_e32 vcc, s51, v29
	v_max3_f32 v18, v18, v8, v9
	s_nop 0
	v_cndmask_b32_e32 v10, v221, v10, vcc
	v_cmp_gt_u32_e32 vcc, s51, v19
	v_subrev_u32_e32 v19, 18, v159
	s_nop 0
	v_cndmask_b32_e32 v11, v221, v11, vcc
	v_cmp_gt_u32_e32 vcc, s51, v19
	v_subrev_u32_e32 v19, 19, v159
	v_max3_f32 v18, v18, v10, v11
	v_cndmask_b32_e32 v12, v221, v12, vcc
	v_cmp_gt_u32_e32 vcc, s51, v19
	v_subrev_u32_e32 v19, 20, v159
	s_nop 0
	v_cndmask_b32_e32 v13, v221, v13, vcc
	v_cmp_gt_u32_e32 vcc, s51, v19
	v_subrev_u32_e32 v19, 21, v159
	v_max3_f32 v18, v18, v12, v13
	v_cndmask_b32_e32 v14, v221, v14, vcc
	v_cmp_gt_u32_e32 vcc, s51, v19
	v_subrev_u32_e32 v19, 22, v159
	s_nop 0
	v_cndmask_b32_e32 v15, v221, v15, vcc
	v_cmp_gt_u32_e32 vcc, s51, v19
	v_subrev_u32_e32 v19, 23, v159
	v_max3_f32 v18, v18, v14, v15
	v_cndmask_b32_e32 v16, v221, v16, vcc
	v_cmp_gt_u32_e32 vcc, s51, v19
	s_nop 1
	v_cndmask_b32_e32 v17, v221, v17, vcc
	v_max3_f32 v18, v18, v16, v17
	v_mov_b32_e32 v19, v18
	s_nop 1
	v_permlane32_swap_b32 v19, v18
	s_waitcnt lgkmcnt(0)
	v_max3_f32 v161, v18, v19, s60
	v_sub_f32_e32 v2, v2, v161
	v_exp_f32_e32 v18, v2
	v_sub_f32_e32 v2, v3, v161
	v_exp_f32_e32 v19, v2
	v_sub_f32_e32 v2, v4, v161
	v_exp_f32_e32 v20, v2
	v_sub_f32_e32 v2, v5, v161
	v_exp_f32_e32 v21, v2
	v_add_f32_e32 v2, 0, v18
	v_add_f32_e32 v2, v19, v2
	v_add_f32_e32 v2, v20, v2
	v_add_f32_e32 v50, v21, v2
	v_sub_f32_e32 v2, v6, v161
	v_exp_f32_e32 v51, v2
	v_sub_f32_e32 v2, v7, v161
	v_exp_f32_e32 v163, v2
	v_sub_f32_e32 v2, v8, v161
	v_exp_f32_e32 v234, v2
	v_sub_f32_e32 v2, v9, v161
	v_exp_f32_e32 v235, v2
	v_sub_f32_e32 v2, v10, v161
	v_exp_f32_e32 v10, v2
	v_sub_f32_e32 v2, v11, v161
	v_exp_f32_e32 v238, v2
	v_sub_f32_e32 v2, v12, v161
	v_sub_f32_e32 v3, 0xefa18f08, v161
	v_exp_f32_e32 v239, v2
	v_sub_f32_e32 v2, v13, v161
	v_exp_f32_e32 v3, v3
	v_exp_f32_e32 v240, v2
	v_sub_f32_e32 v2, v14, v161
	v_exp_f32_e32 v241, v2
	v_sub_f32_e32 v2, v15, v161
	v_cmp_eq_f32_e32 vcc, s60, v161
	v_exp_f32_e32 v242, v2
	v_sub_f32_e32 v2, v16, v161
	s_cmp_lg_u64 vcc, exec
	v_exp_f32_e32 v243, v2
	v_mul_f32_e32 v2, 0, v3
	s_cselect_b64 vcc, -1, 0
	v_cndmask_b32_e32 v34, 0, v2, vcc
	v_add_lshl_u32 v2, s18, v149, 1
	v_mul_u32_u24_e32 v3, 0x310, v55
	v_add3_u32 v12, 0, v2, v3
	ds_read_b128 v[2:5], v12 offset:49152
	ds_read_b128 v[6:9], v12 offset:49184
	v_mov_b32_e32 v35, v34
	v_mov_b32_e32 v36, v34
	v_mov_b32_e32 v37, v34
	v_mov_b32_e32 v38, v34
	v_mov_b32_e32 v39, v34
	v_mov_b32_e32 v40, v34
	v_mov_b32_e32 v41, v34
	v_mov_b32_e32 v42, v34
	v_mov_b32_e32 v43, v34
	v_mov_b32_e32 v44, v34
	v_mov_b32_e32 v45, v34
	v_mov_b32_e32 v46, v34
	v_mov_b32_e32 v47, v34
	v_mov_b32_e32 v48, v34
	v_mov_b32_e32 v49, v34
	v_cvt_pk_bf16_f32 v222, v18, v19
	v_cvt_pk_bf16_f32 v223, v20, v21
	v_cvt_pk_bf16_f32 v224, v51, v163
	v_cvt_pk_bf16_f32 v225, v234, v235
	v_sub_f32_e32 v11, v17, v161
	v_exp_f32_e32 v244, v11
	s_waitcnt lgkmcnt(1)
	v_mfma_f32_32x32x16_bf16 v[18:33], v[2:5], v[222:225], v[34:49]
	v_add_u32_e32 v2, 0xc000, v12
	ds_read_b128 v[230:233], v2 offset:25088
	v_add_f32_e32 v3, v51, v50
	v_add_f32_e32 v3, v163, v3
	v_add_f32_e32 v3, v234, v3
	v_cvt_pk_bf16_f32 v226, v10, v238
	v_cvt_pk_bf16_f32 v227, v239, v240
	v_cvt_pk_bf16_f32 v228, v241, v242
	v_cvt_pk_bf16_f32 v229, v243, v244
	v_add_f32_e32 v3, v235, v3
	v_add_f32_e32 v50, v10, v3
	s_waitcnt lgkmcnt(1)
	v_mfma_f32_32x32x16_bf16 v[18:33], v[6:9], v[226:229], v[18:33]
	ds_read_b128 v[234:237], v2 offset:25120
	v_mov_b64_e32 v[2:3], v[34:35]
	v_mov_b64_e32 v[4:5], v[36:37]
	v_mov_b64_e32 v[6:7], v[38:39]
	v_mov_b64_e32 v[8:9], v[40:41]
	v_mov_b64_e32 v[10:11], v[42:43]
	v_mov_b64_e32 v[12:13], v[44:45]
	v_mov_b64_e32 v[14:15], v[46:47]
	v_mov_b64_e32 v[16:17], v[48:49]
	v_add_f32_e32 v35, v238, v50
	v_add_f32_e32 v35, v239, v35
	s_waitcnt lgkmcnt(1)
	v_mfma_f32_32x32x16_bf16 v[2:17], v[230:233], v[222:225], v[2:17]
	v_add_f32_e32 v35, v240, v35
	v_add_f32_e32 v35, v241, v35
	v_add_f32_e32 v35, v242, v35
	v_add_f32_e32 v35, v243, v35
	v_add_f32_e32 v35, v244, v35
	v_add_f32_e32 v34, v34, v35
	s_waitcnt lgkmcnt(0)
	v_mfma_f32_32x32x16_bf16 v[2:17], v[234:237], v[226:229], v[2:17]
	v_cndmask_b32_e64 v35, 0, 1, s[12:13]
	s_cmp_lt_u32 s43, 3
	v_cmp_ne_u32_e64 s[14:15], 1, v35
	s_cbranch_scc0 .LBB0_1384

.LBB0_1388:
	s_add_i32 s16, s18, 32
	v_or_b32_e32 v163, s16, v151
	v_lshl_add_u32 v230, v163, 7, 0
	v_lshrrev_b32_e32 v163, 1, v163
	v_bitop3_b32 v222, v163, v53, 7 bitop3:0x6c
	v_lshl_add_u32 v222, v222, 4, v230
	ds_read_b128 v[222:225], v222
	v_add_u32_e32 v226, 2, v53
	v_bitop3_b32 v226, v163, v226, 7 bitop3:0x6c
	v_lshl_add_u32 v226, v226, 4, v230
	ds_read_b128 v[226:229], v226
	v_cmp_gt_u32_e32 vcc, s51, v35
	s_waitcnt lgkmcnt(1)
	v_mfma_f32_32x32x16_bf16 v[36:51], v[222:225], v[128:131], v[36:51]
	v_add_u32_e32 v222, 4, v53
	v_bitop3_b32 v222, v163, v222, 7 bitop3:0x6c
	v_lshl_add_u32 v222, v222, 4, v230
	ds_read_b128 v[222:225], v222
	s_waitcnt lgkmcnt(1)
	v_mfma_f32_32x32x16_bf16 v[36:51], v[226:229], v[136:139], v[36:51]
	v_add_u32_e32 v226, 6, v53
	v_bitop3_b32 v163, v163, v226, 7 bitop3:0x6c
	v_lshl_add_u32 v163, v163, 4, v230
	ds_read_b128 v[226:229], v163
	v_subrev_u32_e32 v163, 33, v159
	v_subrev_u32_e32 v230, 38, v159
	s_waitcnt lgkmcnt(1)
	v_mfma_f32_32x32x16_bf16 v[36:51], v[222:225], v[140:143], v[36:51]
	v_subrev_u32_e32 v222, 34, v159
	v_subrev_u32_e32 v223, 35, v159
	v_subrev_u32_e32 v224, 36, v159
	v_subrev_u32_e32 v225, 37, v159
	s_waitcnt lgkmcnt(0)
	v_mfma_f32_32x32x16_bf16 v[36:51], v[226:229], v[132:135], v[36:51]
	s_nop 11
	v_cndmask_b32_e32 v35, v221, v36, vcc
	v_cmp_gt_u32_e32 vcc, s51, v163
	s_nop 1
	v_cndmask_b32_e32 v163, v221, v37, vcc
	v_cmp_gt_u32_e32 vcc, s51, v222
	s_nop 1
	v_cndmask_b32_e32 v222, v221, v38, vcc
	v_cmp_gt_u32_e32 vcc, s51, v223
	v_cndmask_b32_e64 v223, v37, v163, s[10:11]
	v_cndmask_b32_e64 v222, v38, v222, s[10:11]
	v_cndmask_b32_e32 v226, v221, v39, vcc
	v_cmp_gt_u32_e32 vcc, s51, v224
	v_cndmask_b32_e64 v224, v36, v35, s[10:11]
	v_cndmask_b32_e64 v163, v39, v226, s[10:11]
	v_cndmask_b32_e32 v227, v221, v40, vcc
	v_cmp_gt_u32_e32 vcc, s51, v225
	v_cndmask_b32_e64 v39, v40, v227, s[10:11]
	v_max3_f32 v35, v224, s60, v223
	v_cndmask_b32_e32 v225, v221, v41, vcc
	v_cmp_gt_u32_e32 vcc, s51, v230
	v_cndmask_b32_e64 v38, v41, v225, s[10:11]
	v_max3_f32 v35, v35, v222, v163
	v_cndmask_b32_e32 v36, v221, v42, vcc
	v_cndmask_b32_e64 v40, v42, v36, s[10:11]
	v_subrev_u32_e32 v36, 39, v159
	v_cmp_gt_u32_e32 vcc, s51, v36
	v_max3_f32 v35, v35, v39, v38
	v_subrev_u32_e32 v37, 55, v159
	v_cndmask_b32_e32 v36, v221, v43, vcc
	v_cndmask_b32_e64 v41, v43, v36, s[10:11]
	v_subrev_u32_e32 v36, 48, v159
	v_cmp_gt_u32_e32 vcc, s51, v36
	v_max3_f32 v35, v35, v40, v41
	s_nop 0
	v_cndmask_b32_e32 v36, v221, v44, vcc
	v_cndmask_b32_e64 v42, v44, v36, s[10:11]
	v_subrev_u32_e32 v36, 49, v159
	v_cmp_gt_u32_e32 vcc, s51, v36
	s_nop 1
	v_cndmask_b32_e32 v36, v221, v45, vcc
	v_cndmask_b32_e64 v43, v45, v36, s[10:11]
	v_subrev_u32_e32 v36, 50, v159
	v_cmp_gt_u32_e32 vcc, s51, v36
	v_max3_f32 v35, v35, v42, v43
	s_nop 0
	v_cndmask_b32_e32 v36, v221, v46, vcc
	v_cndmask_b32_e64 v44, v46, v36, s[10:11]
	v_subrev_u32_e32 v36, 51, v159
	v_cmp_gt_u32_e32 vcc, s51, v36
	s_nop 1
	v_cndmask_b32_e32 v36, v221, v47, vcc
	v_cndmask_b32_e64 v45, v47, v36, s[10:11]
	v_subrev_u32_e32 v36, 52, v159
	v_cmp_gt_u32_e32 vcc, s51, v36
	v_max3_f32 v35, v35, v44, v45
	s_nop 0
	v_cndmask_b32_e32 v36, v221, v48, vcc
	v_cndmask_b32_e64 v46, v48, v36, s[10:11]
	v_subrev_u32_e32 v36, 53, v159
	v_cmp_gt_u32_e32 vcc, s51, v36
	s_nop 1
	v_cndmask_b32_e32 v36, v221, v49, vcc
	v_cndmask_b32_e64 v47, v49, v36, s[10:11]
	v_subrev_u32_e32 v36, 54, v159
	v_cmp_gt_u32_e32 vcc, s51, v36
	v_max3_f32 v35, v35, v46, v47
	s_nop 0
	v_cndmask_b32_e32 v36, v221, v50, vcc
	v_cmp_gt_u32_e32 vcc, s51, v37
	v_cndmask_b32_e64 v36, v50, v36, s[10:11]
	s_nop 0
	v_cndmask_b32_e32 v37, v221, v51, vcc
	v_cndmask_b32_e64 v37, v51, v37, s[10:11]
	v_max3_f32 v35, v35, v36, v37
	v_mov_b32_e32 v48, v35
	s_nop 1
	v_permlane32_swap_b32 v48, v35
	s_waitcnt lgkmcnt(0)
	v_max3_f32 v35, v161, v35, v48
	v_cmp_eq_f32_e32 vcc, v35, v161
	s_cmp_eq_u64 vcc, exec
	s_cbranch_scc1 .LBB0_1390
	v_sub_f32_e32 v48, v161, v35
	v_exp_f32_e32 v48, v48
	s_nop 0
	v_pk_mul_f32 v[32:33], v[32:33], v[48:49] op_sel_hi:[1,0]
	v_pk_mul_f32 v[30:31], v[30:31], v[48:49] op_sel_hi:[1,0]
	v_pk_mul_f32 v[28:29], v[28:29], v[48:49] op_sel_hi:[1,0]
	v_pk_mul_f32 v[26:27], v[26:27], v[48:49] op_sel_hi:[1,0]
	v_pk_mul_f32 v[24:25], v[24:25], v[48:49] op_sel_hi:[1,0]
	v_pk_mul_f32 v[22:23], v[22:23], v[48:49] op_sel_hi:[1,0]
	v_pk_mul_f32 v[20:21], v[20:21], v[48:49] op_sel_hi:[1,0]
	v_pk_mul_f32 v[18:19], v[18:19], v[48:49] op_sel_hi:[1,0]
	v_pk_mul_f32 v[16:17], v[16:17], v[48:49] op_sel_hi:[1,0]
	v_pk_mul_f32 v[14:15], v[14:15], v[48:49] op_sel_hi:[1,0]
	v_pk_mul_f32 v[12:13], v[12:13], v[48:49] op_sel_hi:[1,0]
	v_pk_mul_f32 v[10:11], v[10:11], v[48:49] op_sel_hi:[1,0]
	v_pk_mul_f32 v[8:9], v[8:9], v[48:49] op_sel_hi:[1,0]
	v_pk_mul_f32 v[6:7], v[6:7], v[48:49] op_sel_hi:[1,0]
	v_pk_mul_f32 v[4:5], v[4:5], v[48:49] op_sel_hi:[1,0]
	v_pk_mul_f32 v[2:3], v[2:3], v[48:49] op_sel_hi:[1,0]
	v_mul_f32_e32 v34, v34, v48

.LBB0_1395:
	s_add_i32 s16, s18, 64
	v_or_b32_e32 v163, s16, v151
	v_lshl_add_u32 v230, v163, 7, 0
	v_lshrrev_b32_e32 v163, 1, v163
	v_bitop3_b32 v222, v163, v53, 7 bitop3:0x6c
	v_lshl_add_u32 v222, v222, 4, v230
	ds_read_b128 v[222:225], v222
	v_add_u32_e32 v226, 2, v53
	v_bitop3_b32 v226, v163, v226, 7 bitop3:0x6c
	v_lshl_add_u32 v226, v226, 4, v230
	ds_read_b128 v[226:229], v226
	v_cmp_gt_u32_e32 vcc, s51, v161
	s_waitcnt lgkmcnt(1)
	v_mfma_f32_32x32x16_bf16 v[36:51], v[222:225], v[128:131], v[36:51]
	v_add_u32_e32 v222, 4, v53
	v_bitop3_b32 v222, v163, v222, 7 bitop3:0x6c
	v_lshl_add_u32 v222, v222, 4, v230
	ds_read_b128 v[222:225], v222
	s_waitcnt lgkmcnt(1)
	v_mfma_f32_32x32x16_bf16 v[36:51], v[226:229], v[136:139], v[36:51]
	v_add_u32_e32 v226, 6, v53
	v_bitop3_b32 v163, v163, v226, 7 bitop3:0x6c
	v_lshl_add_u32 v163, v163, 4, v230
	ds_read_b128 v[226:229], v163
	v_add_u32_e32 v163, 0xffffffbf, v159
	v_add_u32_e32 v230, 0xffffffba, v159
	s_waitcnt lgkmcnt(1)
	v_mfma_f32_32x32x16_bf16 v[36:51], v[222:225], v[140:143], v[36:51]
	v_add_u32_e32 v222, 0xffffffbe, v159
	v_add_u32_e32 v223, 0xffffffbd, v159
	v_add_u32_e32 v224, 0xffffffbc, v159
	v_add_u32_e32 v225, 0xffffffbb, v159
	s_waitcnt lgkmcnt(0)
	v_mfma_f32_32x32x16_bf16 v[36:51], v[226:229], v[132:135], v[36:51]
	s_nop 11
	v_cndmask_b32_e32 v161, v221, v36, vcc
	v_cmp_gt_u32_e32 vcc, s51, v163
	s_nop 1
	v_cndmask_b32_e32 v163, v221, v37, vcc
	v_cmp_gt_u32_e32 vcc, s51, v222
	s_nop 1
	v_cndmask_b32_e32 v222, v221, v38, vcc
	v_cmp_gt_u32_e32 vcc, s51, v223
	v_cndmask_b32_e64 v223, v37, v163, s[10:11]
	v_cndmask_b32_e64 v222, v38, v222, s[10:11]
	v_cndmask_b32_e32 v226, v221, v39, vcc
	v_cmp_gt_u32_e32 vcc, s51, v224
	v_cndmask_b32_e64 v163, v39, v226, s[10:11]
	v_cndmask_b32_e64 v224, v36, v161, s[10:11]
	v_cndmask_b32_e32 v227, v221, v40, vcc
	v_cmp_gt_u32_e32 vcc, s51, v225
	v_cndmask_b32_e64 v39, v40, v227, s[10:11]
	v_max3_f32 v36, v224, s60, v223
	v_cndmask_b32_e32 v225, v221, v41, vcc
	v_cmp_gt_u32_e32 vcc, s51, v230
	v_cndmask_b32_e64 v38, v41, v225, s[10:11]
	v_max3_f32 v36, v36, v222, v163
	v_cndmask_b32_e32 v37, v221, v42, vcc
	v_cndmask_b32_e64 v40, v42, v37, s[10:11]
	v_add_u32_e32 v37, 0xffffffb9, v159
	v_cmp_gt_u32_e32 vcc, s51, v37
	v_max3_f32 v36, v36, v39, v38
	s_nop 0
	v_cndmask_b32_e32 v37, v221, v43, vcc
	v_cndmask_b32_e64 v41, v43, v37, s[10:11]
	v_add_u32_e32 v37, 0xffffffb0, v159
	v_cmp_gt_u32_e32 vcc, s51, v37
	v_max3_f32 v36, v36, v40, v41
	s_nop 0
	v_cndmask_b32_e32 v37, v221, v44, vcc
	v_cndmask_b32_e64 v42, v44, v37, s[10:11]
	v_add_u32_e32 v37, 0xffffffaf, v159
	v_cmp_gt_u32_e32 vcc, s51, v37
	s_nop 1
	v_cndmask_b32_e32 v37, v221, v45, vcc
	v_cndmask_b32_e64 v43, v45, v37, s[10:11]
	v_add_u32_e32 v37, 0xffffffae, v159
	v_cmp_gt_u32_e32 vcc, s51, v37
	v_max3_f32 v36, v36, v42, v43
	s_nop 0
	v_cndmask_b32_e32 v37, v221, v46, vcc
	v_cndmask_b32_e64 v44, v46, v37, s[10:11]
	v_add_u32_e32 v37, 0xffffffad, v159
	v_cmp_gt_u32_e32 vcc, s51, v37
	s_nop 1
	v_cndmask_b32_e32 v37, v221, v47, vcc
	v_cndmask_b32_e64 v45, v47, v37, s[10:11]
	v_add_u32_e32 v37, 0xffffffac, v159
	v_cmp_gt_u32_e32 vcc, s51, v37
	v_max3_f32 v36, v36, v44, v45
	s_nop 0
	v_cndmask_b32_e32 v37, v221, v48, vcc
	v_cndmask_b32_e64 v46, v48, v37, s[10:11]
	v_add_u32_e32 v37, 0xffffffab, v159
	v_cmp_gt_u32_e32 vcc, s51, v37
	s_nop 1
	v_cndmask_b32_e32 v37, v221, v49, vcc
	v_cndmask_b32_e64 v47, v49, v37, s[10:11]
	v_max3_f32 v48, v36, v46, v47
	v_add_u32_e32 v36, 0xffffffaa, v159
	v_cmp_gt_u32_e32 vcc, s51, v36
	v_add_u32_e32 v37, 0xffffffa9, v159
	s_nop 0
	v_cndmask_b32_e32 v36, v221, v50, vcc
	v_cmp_gt_u32_e32 vcc, s51, v37
	v_cndmask_b32_e64 v36, v50, v36, s[10:11]
	s_nop 0
	v_cndmask_b32_e32 v37, v221, v51, vcc
	v_cndmask_b32_e64 v37, v51, v37, s[10:11]
	v_max3_f32 v48, v48, v36, v37
	v_mov_b32_e32 v49, v48
	s_nop 1
	v_permlane32_swap_b32 v49, v48
	s_waitcnt lgkmcnt(0)
	v_max3_f32 v161, v35, v48, v49
	v_cmp_eq_f32_e32 vcc, v161, v35
	s_cmp_eq_u64 vcc, exec
	s_cbranch_scc1 .LBB0_1397
	v_sub_f32_e32 v35, v35, v161
	v_exp_f32_e32 v48, v35
	s_nop 0
	v_pk_mul_f32 v[32:33], v[32:33], v[48:49] op_sel_hi:[1,0]
	v_pk_mul_f32 v[30:31], v[30:31], v[48:49] op_sel_hi:[1,0]
	v_pk_mul_f32 v[28:29], v[28:29], v[48:49] op_sel_hi:[1,0]
	v_pk_mul_f32 v[26:27], v[26:27], v[48:49] op_sel_hi:[1,0]
	v_pk_mul_f32 v[24:25], v[24:25], v[48:49] op_sel_hi:[1,0]
	v_pk_mul_f32 v[22:23], v[22:23], v[48:49] op_sel_hi:[1,0]
	v_pk_mul_f32 v[20:21], v[20:21], v[48:49] op_sel_hi:[1,0]
	v_pk_mul_f32 v[18:19], v[18:19], v[48:49] op_sel_hi:[1,0]
	v_pk_mul_f32 v[16:17], v[16:17], v[48:49] op_sel_hi:[1,0]
	v_pk_mul_f32 v[14:15], v[14:15], v[48:49] op_sel_hi:[1,0]
	v_pk_mul_f32 v[12:13], v[12:13], v[48:49] op_sel_hi:[1,0]
	v_pk_mul_f32 v[10:11], v[10:11], v[48:49] op_sel_hi:[1,0]
	v_pk_mul_f32 v[8:9], v[8:9], v[48:49] op_sel_hi:[1,0]
	v_pk_mul_f32 v[6:7], v[6:7], v[48:49] op_sel_hi:[1,0]
	v_pk_mul_f32 v[4:5], v[4:5], v[48:49] op_sel_hi:[1,0]
	v_pk_mul_f32 v[2:3], v[2:3], v[48:49] op_sel_hi:[1,0]
	v_mul_f32_e32 v34, v34, v48

.LBB0_1402:
	s_add_i32 s16, s18, 0x60
	v_or_b32_e32 v163, s16, v151
	v_lshl_add_u32 v230, v163, 7, 0
	v_lshrrev_b32_e32 v163, 1, v163
	v_bitop3_b32 v222, v163, v53, 7 bitop3:0x6c
	v_lshl_add_u32 v222, v222, 4, v230
	ds_read_b128 v[222:225], v222
	v_add_u32_e32 v226, 2, v53
	v_bitop3_b32 v226, v163, v226, 7 bitop3:0x6c
	v_lshl_add_u32 v226, v226, 4, v230
	ds_read_b128 v[226:229], v226
	v_cmp_gt_u32_e32 vcc, s51, v35
	s_waitcnt lgkmcnt(1)
	v_mfma_f32_32x32x16_bf16 v[36:51], v[222:225], v[128:131], v[36:51]
	v_add_u32_e32 v222, 4, v53
	v_bitop3_b32 v222, v163, v222, 7 bitop3:0x6c
	v_lshl_add_u32 v222, v222, 4, v230
	ds_read_b128 v[222:225], v222
	s_waitcnt lgkmcnt(1)
	v_mfma_f32_32x32x16_bf16 v[36:51], v[226:229], v[136:139], v[36:51]
	v_add_u32_e32 v226, 6, v53
	v_bitop3_b32 v163, v163, v226, 7 bitop3:0x6c
	v_lshl_add_u32 v163, v163, 4, v230
	ds_read_b128 v[226:229], v163
	v_add_u32_e32 v163, 0xffffff9f, v159
	v_add_u32_e32 v230, 0xffffff9a, v159
	s_waitcnt lgkmcnt(1)
	v_mfma_f32_32x32x16_bf16 v[36:51], v[222:225], v[140:143], v[36:51]
	v_add_u32_e32 v222, 0xffffff9e, v159
	v_add_u32_e32 v223, 0xffffff9d, v159
	v_add_u32_e32 v224, 0xffffff9c, v159
	v_add_u32_e32 v225, 0xffffff9b, v159
	s_waitcnt lgkmcnt(0)
	v_mfma_f32_32x32x16_bf16 v[36:51], v[226:229], v[132:135], v[36:51]
	s_nop 11
	v_cndmask_b32_e32 v35, v221, v36, vcc
	v_cmp_gt_u32_e32 vcc, s51, v163
	s_nop 1
	v_cndmask_b32_e32 v163, v221, v37, vcc
	v_cmp_gt_u32_e32 vcc, s51, v222
	s_nop 1
	v_cndmask_b32_e32 v222, v221, v38, vcc
	v_cmp_gt_u32_e32 vcc, s51, v223
	v_cndmask_b32_e64 v223, v37, v163, s[10:11]
	v_cndmask_b32_e64 v222, v38, v222, s[10:11]
	v_cndmask_b32_e32 v226, v221, v39, vcc
	v_cmp_gt_u32_e32 vcc, s51, v224
	v_cndmask_b32_e64 v224, v36, v35, s[10:11]
	v_cndmask_b32_e64 v163, v39, v226, s[10:11]
	v_cndmask_b32_e32 v227, v221, v40, vcc
	v_cmp_gt_u32_e32 vcc, s51, v225
	v_cndmask_b32_e64 v39, v40, v227, s[10:11]
	v_max3_f32 v35, v224, s60, v223
	v_cndmask_b32_e32 v225, v221, v41, vcc
	v_cmp_gt_u32_e32 vcc, s51, v230
	v_cndmask_b32_e64 v38, v41, v225, s[10:11]
	v_max3_f32 v35, v35, v222, v163
	v_cndmask_b32_e32 v36, v221, v42, vcc
	v_cndmask_b32_e64 v40, v42, v36, s[10:11]
	v_add_u32_e32 v36, 0xffffff99, v159
	v_cmp_gt_u32_e32 vcc, s51, v36
	v_max3_f32 v35, v35, v39, v38
	v_add_u32_e32 v37, 0xffffff89, v159
	v_cndmask_b32_e32 v36, v221, v43, vcc
	v_cndmask_b32_e64 v41, v43, v36, s[10:11]
	v_add_u32_e32 v36, 0xffffff90, v159
	v_cmp_gt_u32_e32 vcc, s51, v36
	v_max3_f32 v35, v35, v40, v41
	s_nop 0
	v_cndmask_b32_e32 v36, v221, v44, vcc
	v_cndmask_b32_e64 v42, v44, v36, s[10:11]
	v_add_u32_e32 v36, 0xffffff8f, v159
	v_cmp_gt_u32_e32 vcc, s51, v36
	s_nop 1
	v_cndmask_b32_e32 v36, v221, v45, vcc
	v_cndmask_b32_e64 v43, v45, v36, s[10:11]
	v_add_u32_e32 v36, 0xffffff8e, v159
	v_cmp_gt_u32_e32 vcc, s51, v36
	v_max3_f32 v35, v35, v42, v43
	s_nop 0
	v_cndmask_b32_e32 v36, v221, v46, vcc
	v_cndmask_b32_e64 v44, v46, v36, s[10:11]
	v_add_u32_e32 v36, 0xffffff8d, v159
	v_cmp_gt_u32_e32 vcc, s51, v36
	s_nop 1
	v_cndmask_b32_e32 v36, v221, v47, vcc
	v_cndmask_b32_e64 v45, v47, v36, s[10:11]
	v_add_u32_e32 v36, 0xffffff8c, v159
	v_cmp_gt_u32_e32 vcc, s51, v36
	v_max3_f32 v35, v35, v44, v45
	s_nop 0
	v_cndmask_b32_e32 v36, v221, v48, vcc
	v_cndmask_b32_e64 v46, v48, v36, s[10:11]
	v_add_u32_e32 v36, 0xffffff8b, v159
	v_cmp_gt_u32_e32 vcc, s51, v36
	s_nop 1
	v_cndmask_b32_e32 v36, v221, v49, vcc
	v_cndmask_b32_e64 v47, v49, v36, s[10:11]
	v_add_u32_e32 v36, 0xffffff8a, v159
	v_cmp_gt_u32_e32 vcc, s51, v36
	v_max3_f32 v35, v35, v46, v47
	s_nop 0
	v_cndmask_b32_e32 v36, v221, v50, vcc
	v_cmp_gt_u32_e32 vcc, s51, v37
	v_cndmask_b32_e64 v36, v50, v36, s[10:11]
	s_nop 0
	v_cndmask_b32_e32 v37, v221, v51, vcc
	v_cndmask_b32_e64 v37, v51, v37, s[10:11]
	v_max3_f32 v35, v35, v36, v37
	v_mov_b32_e32 v48, v35
	s_nop 1
	v_permlane32_swap_b32 v48, v35
	s_waitcnt lgkmcnt(0)
	v_max3_f32 v35, v161, v35, v48
	v_cmp_eq_f32_e32 vcc, v35, v161
	s_cmp_eq_u64 vcc, exec
	s_cbranch_scc1 .LBB0_1404
	v_sub_f32_e32 v48, v161, v35
	v_exp_f32_e32 v48, v48
	s_nop 0
	v_pk_mul_f32 v[32:33], v[32:33], v[48:49] op_sel_hi:[1,0]
	v_pk_mul_f32 v[30:31], v[30:31], v[48:49] op_sel_hi:[1,0]
	v_pk_mul_f32 v[28:29], v[28:29], v[48:49] op_sel_hi:[1,0]
	v_pk_mul_f32 v[26:27], v[26:27], v[48:49] op_sel_hi:[1,0]
	v_pk_mul_f32 v[24:25], v[24:25], v[48:49] op_sel_hi:[1,0]
	v_pk_mul_f32 v[22:23], v[22:23], v[48:49] op_sel_hi:[1,0]
	v_pk_mul_f32 v[20:21], v[20:21], v[48:49] op_sel_hi:[1,0]
	v_pk_mul_f32 v[18:19], v[18:19], v[48:49] op_sel_hi:[1,0]
	v_pk_mul_f32 v[16:17], v[16:17], v[48:49] op_sel_hi:[1,0]
	v_pk_mul_f32 v[14:15], v[14:15], v[48:49] op_sel_hi:[1,0]
	v_pk_mul_f32 v[12:13], v[12:13], v[48:49] op_sel_hi:[1,0]
	v_pk_mul_f32 v[10:11], v[10:11], v[48:49] op_sel_hi:[1,0]
	v_pk_mul_f32 v[8:9], v[8:9], v[48:49] op_sel_hi:[1,0]
	v_pk_mul_f32 v[6:7], v[6:7], v[48:49] op_sel_hi:[1,0]
	v_pk_mul_f32 v[4:5], v[4:5], v[48:49] op_sel_hi:[1,0]
	v_pk_mul_f32 v[2:3], v[2:3], v[48:49] op_sel_hi:[1,0]
	v_mul_f32_e32 v34, v34, v48

.LBB0_1408:
	s_addk_i32 s18, 0x80
	v_or_b32_e32 v151, s18, v151
	s_waitcnt lgkmcnt(0)
	v_lshl_add_u32 v157, v151, 7, 0
	v_lshrrev_b32_e32 v151, 1, v151
	v_bitop3_b32 v161, v151, v53, 7 bitop3:0x6c
	v_lshl_add_u32 v161, v161, 4, v157
	ds_read_b128 v[222:225], v161
	v_add_u32_e32 v161, 2, v53
	v_bitop3_b32 v161, v151, v161, 7 bitop3:0x6c
	v_lshl_add_u32 v161, v161, 4, v157
	ds_read_b128 v[226:229], v161
	v_add_u32_e32 v161, -1, v159
	v_cmp_gt_u32_e32 vcc, s51, v159
	s_waitcnt lgkmcnt(1)
	v_mfma_f32_32x32x16_bf16 v[36:51], v[222:225], v[128:131], v[36:51]
	v_add_u32_e32 v128, 4, v53
	v_bitop3_b32 v128, v151, v128, 7 bitop3:0x6c
	v_lshl_add_u32 v128, v128, 4, v157
	ds_read_b128 v[128:131], v128
	s_waitcnt lgkmcnt(1)
	v_mfma_f32_32x32x16_bf16 v[36:51], v[226:229], v[136:139], v[36:51]
	v_add_u32_e32 v136, 6, v53
	v_bitop3_b32 v136, v151, v136, 7 bitop3:0x6c
	v_lshl_add_u32 v136, v136, 4, v157
	ds_read_b128 v[136:139], v136
	s_waitcnt lgkmcnt(1)
	v_mfma_f32_32x32x16_bf16 v[36:51], v[128:131], v[140:143], v[36:51]
	v_add_u32_e32 v128, -2, v159
	v_add_u32_e32 v129, -3, v159
	v_add_u32_e32 v130, -4, v159
	v_add_u32_e32 v140, -5, v159
	v_add_u32_e32 v141, -6, v159
	v_add_u32_e32 v142, -7, v159
	v_add_u32_e32 v143, -16, v159
	s_waitcnt lgkmcnt(0)
	v_mfma_f32_32x32x16_bf16 v[36:51], v[136:139], v[132:135], v[36:51]
	s_nop 11
	v_cndmask_b32_e32 v134, v221, v36, vcc
	v_cmp_gt_u32_e32 vcc, s51, v161
	s_nop 1
	v_cndmask_b32_e32 v133, v221, v37, vcc
	v_cmp_gt_u32_e32 vcc, s51, v128
	v_subrev_u32_e32 v37, 17, v159
	v_max3_f32 v36, v134, s60, v133
	v_cndmask_b32_e32 v132, v221, v38, vcc
	v_cmp_gt_u32_e32 vcc, s51, v129
	v_subrev_u32_e32 v38, 23, v159
	s_nop 0
	v_cndmask_b32_e32 v131, v221, v39, vcc
	v_cmp_gt_u32_e32 vcc, s51, v130
	v_max3_f32 v36, v36, v132, v131
	s_nop 0
	v_cndmask_b32_e32 v130, v221, v40, vcc
	v_cmp_gt_u32_e32 vcc, s51, v140
	s_nop 1
	v_cndmask_b32_e32 v129, v221, v41, vcc
	v_cmp_gt_u32_e32 vcc, s51, v141
	v_max3_f32 v36, v36, v130, v129
	s_nop 0
	v_cndmask_b32_e32 v40, v221, v42, vcc
	v_cmp_gt_u32_e32 vcc, s51, v142
	s_nop 1
	v_cndmask_b32_e32 v39, v221, v43, vcc
	v_cmp_gt_u32_e32 vcc, s51, v143
	v_max3_f32 v36, v36, v40, v39
	s_nop 0
	v_cndmask_b32_e32 v128, v221, v44, vcc
	v_cmp_gt_u32_e32 vcc, s51, v37
	v_subrev_u32_e32 v37, 18, v159
	s_nop 0
	v_cndmask_b32_e32 v45, v221, v45, vcc
	v_cmp_gt_u32_e32 vcc, s51, v37
	v_subrev_u32_e32 v37, 19, v159
	v_max3_f32 v36, v36, v128, v45
	v_cndmask_b32_e32 v41, v221, v46, vcc
	v_cmp_gt_u32_e32 vcc, s51, v37
	v_subrev_u32_e32 v37, 20, v159
	s_nop 0
	v_cndmask_b32_e32 v42, v221, v47, vcc
	v_cmp_gt_u32_e32 vcc, s51, v37
	v_subrev_u32_e32 v37, 21, v159
	v_max3_f32 v36, v36, v41, v42
	v_cndmask_b32_e32 v43, v221, v48, vcc
	v_cmp_gt_u32_e32 vcc, s51, v37
	v_subrev_u32_e32 v37, 22, v159
	s_nop 0
	v_cndmask_b32_e32 v44, v221, v49, vcc
	v_cmp_gt_u32_e32 vcc, s51, v37
	v_max3_f32 v36, v36, v43, v44
	s_nop 0
	v_cndmask_b32_e32 v37, v221, v50, vcc
	v_cmp_gt_u32_e32 vcc, s51, v38
	s_nop 1
	v_cndmask_b32_e32 v38, v221, v51, vcc
	v_max3_f32 v36, v36, v37, v38
	v_mov_b32_e32 v46, v36
	s_nop 1
	v_permlane32_swap_b32 v46, v36
	s_waitcnt lgkmcnt(0)
	v_max3_f32 v36, v35, v36, v46
	v_cmp_eq_f32_e32 vcc, v36, v35
	s_cmp_eq_u64 vcc, exec
	s_cbranch_scc1 .LBB0_1410
	v_sub_f32_e32 v35, v35, v36
	v_exp_f32_e32 v46, v35
	s_nop 0
	v_pk_mul_f32 v[32:33], v[32:33], v[46:47] op_sel_hi:[1,0]
	v_pk_mul_f32 v[30:31], v[30:31], v[46:47] op_sel_hi:[1,0]
	v_pk_mul_f32 v[28:29], v[28:29], v[46:47] op_sel_hi:[1,0]
	v_pk_mul_f32 v[26:27], v[26:27], v[46:47] op_sel_hi:[1,0]
	v_pk_mul_f32 v[24:25], v[24:25], v[46:47] op_sel_hi:[1,0]
	v_pk_mul_f32 v[22:23], v[22:23], v[46:47] op_sel_hi:[1,0]
	v_pk_mul_f32 v[20:21], v[20:21], v[46:47] op_sel_hi:[1,0]
	v_pk_mul_f32 v[18:19], v[18:19], v[46:47] op_sel_hi:[1,0]
	v_pk_mul_f32 v[16:17], v[16:17], v[46:47] op_sel_hi:[1,0]
	v_pk_mul_f32 v[14:15], v[14:15], v[46:47] op_sel_hi:[1,0]
	v_pk_mul_f32 v[12:13], v[12:13], v[46:47] op_sel_hi:[1,0]
	v_pk_mul_f32 v[10:11], v[10:11], v[46:47] op_sel_hi:[1,0]
	v_pk_mul_f32 v[8:9], v[8:9], v[46:47] op_sel_hi:[1,0]
	v_pk_mul_f32 v[6:7], v[6:7], v[46:47] op_sel_hi:[1,0]
	v_pk_mul_f32 v[4:5], v[4:5], v[46:47] op_sel_hi:[1,0]
	v_pk_mul_f32 v[2:3], v[2:3], v[46:47] op_sel_hi:[1,0]
	v_mul_f32_e32 v34, v34, v46
